# baseline (speedup 1.0000x reference)
.Lprio_skip:
	s_waitcnt lgkmcnt(0)
	global_load_dword v32, v4, s[18:19]
	global_load_dword v33, v4, s[20:21]
	global_load_dword v34, v4, s[22:23]
	global_load_dword v35, v4, s[24:25]
	global_load_dword v36, v4, s[14:15]
	global_load_dword v37, v4, s[16:17]
	s_add_u32 s12, s12, s8
	s_addc_u32 s13, s13, s9
	global_load_dwordx4 v[128:131], v6, s[12:13] offset:0 nt
	global_load_dwordx4 v[132:135], v6, s[12:13] offset:1024 nt
	global_load_dwordx4 v[136:139], v6, s[12:13] offset:2048 nt
	global_load_dwordx4 v[140:143], v6, s[12:13] offset:3072 nt
	v_add_u32_e32 v6, 0x8000, v6
	global_load_dwordx4 v[144:147], v6, s[12:13] offset:0 nt
	global_load_dwordx4 v[148:151], v6, s[12:13] offset:1024 nt
	global_load_dwordx4 v[152:155], v6, s[12:13] offset:2048 nt
	global_load_dwordx4 v[156:159], v6, s[12:13] offset:3072 nt
	s_cmp_ge_u32 s28, 4
	s_cbranch_scc0 .Lstag_skip
	s_sleep 8
